# P12: hipcc's loop-top vmcnt(0) store drain hoisted in front of the loop so the next token's loads issue while the previous token's output stores drain
# baseline (speedup 1.0000x reference)
; #define GAS __attribute__((address_space(1)))
; #define LAS __attribute__((address_space(3)))
; __global__ void __launch_bounds__(NTHR, 2) mk_fwd(Args args) {
;     ...
;         LAS float* s_lnw = (LAS float*)lds; LAS float* s_lnb = s_lnw + 2048;
;         *(LAS f32x4*)(s_lnw + 4 * tid) = *(const GAS f32x4*)(ln2_w + 4 * tid); *(LAS f32x4*)(s_lnb + 4 * tid) = *(const GAS f32x4*)(ln2_b + 4 * tid);
;         __syncthreads();
;         int nsl[4]; float ngt[4];
; #pragma unroll
;         for (int k = 0; k < 4; ++k) { nsl[k] = SLOT_OF[gw * 4 + k]; ngt[k] = GATE[gw * 4 + k]; }
; #pragma unroll 1
;         for (int m = gw; m < M; m += NGW) {
;             int sl[4]; float gt[4];
; #pragma unroll
;             for (int k = 0; k < 4; ++k) { sl[k] = nsl[k]; gt[k] = ngt[k]; }
;             { const int mn = m + NGW < M ? m + NGW : m;
; #pragma unroll
;               for (int k = 0; k < 4; ++k) { nsl[k] = SLOT_OF[mn * 4 + k]; ngt[k] = GATE[mn * 4 + k]; } }
;             f32x4 v[8]; float s = 0.f;
; #pragma unroll
;             for (int q = 0; q < 8; ++q) { const int c = 4 * lane + 256 * q; f32x4 f = (f32x4){0.f, 0.f, 0.f, 0.f};
; #pragma unroll
;                 for (int k = 0; k < 4; ++k) { const unsigned yv = *(const GAS unsigned*)(YS + (size_t)sl[k] * D + c); const f32x2n lo2 = __builtin_amdgcn_cvt_pk_f32_fp8(yv, false), hi2 = __builtin_amdgcn_cvt_pk_f32_fp8(yv, true); f += (gt[k] * (1.0f / pg8::YS_SCALE)) * (f32x4){lo2.x, lo2.y, hi2.x, hi2.y}; }
;                 { const v2u hw = *(const GAS v2u*)(H + (size_t)m * D + c); v[q] = ALPHA * (f32x4){bflo(hw.x), bfhi(hw.x), bflo(hw.y), bfhi(hw.y)} + f; } s += (v[q].x + v[q].y) + (v[q].z + v[q].w); }
.LBB0_1216:
	s_cmp_lt_i32 s88, 13
	s_cselect_b64 s[0:1], -1, 0
	s_and_b64 s[0:1], s[0:1], s[2:3]
	s_andn2_b64 vcc, exec, s[0:1]
	s_cbranch_vccnz .LBB0_1220
	s_waitcnt vmcnt(0)
	v_lshlrev_b32_e32 v8, 2, v195
	global_load_dwordx4 v[0:3], v8, s[20:21]
	global_load_dwordx4 v[4:7], v8, s[22:23]
	s_cmpk_gt_i32 s30, 0x3fff
	v_add_u32_e32 v8, 0, v8
	s_waitcnt vmcnt(0)
	ds_write_b128 v8, v[0:3]
	ds_write_b128 v8, v[4:7] offset:8192
	s_waitcnt lgkmcnt(0)
	s_barrier
	s_cbranch_scc1 .LBB0_1220
	s_lshl_b32 s0, s30, 2
	s_ashr_i32 s1, s0, 31
	s_lshl_b64 s[0:1], s[0:1], 2
	s_add_u32 s2, s66, s0
	s_addc_u32 s3, s67, s1
	v_mov_b32_e32 v73, 0
	s_add_u32 s0, s4, s0
	s_addc_u32 s1, s5, s1
	global_load_dwordx4 v[68:71], v73, s[2:3]
	global_load_dwordx4 v[64:67], v73, s[0:1]
	v_lshlrev_b32_e32 v0, 2, v194
	v_mov_b32_e32 v1, v73
	v_lshl_add_u32 v60, v194, 4, 0
	v_lshl_add_u64 v[74:75], s[8:9], 0, v[0:1]
	v_or_b32_e32 v72, 0x100, v0
	v_or_b32_e32 v76, 0x200, v0
	v_or_b32_e32 v78, 0x300, v0
	v_or_b32_e32 v80, 0x400, v0
	v_or_b32_e32 v82, 0x500, v0
	v_or_b32_e32 v84, 0x600, v0
	v_or_b32_e32 v86, 0x700, v0
	ds_read_b128 v[0:3], v60
	ds_read_b128 v[4:7], v60 offset:1024
	ds_read_b128 v[8:11], v60 offset:8192
	ds_read_b128 v[12:15], v60 offset:9216
	ds_read_b128 v[16:19], v60 offset:2048
	ds_read_b128 v[20:23], v60 offset:3072
	ds_read_b128 v[24:27], v60 offset:10240
	ds_read_b128 v[28:31], v60 offset:11264
	ds_read_b128 v[32:35], v60 offset:4096
	ds_read_b128 v[36:39], v60 offset:5120
	ds_read_b128 v[40:43], v60 offset:12288
	ds_read_b128 v[44:47], v60 offset:13312
	ds_read_b128 v[48:51], v60 offset:6144
	ds_read_b128 v[52:55], v60 offset:7168
	ds_read_b128 v[56:59], v60 offset:14336
	ds_read_b128 v[60:63], v60 offset:15360
	s_ashr_i32 s31, s30, 31
	s_lshl_b64 s[0:1], s[30:31], 13
	s_add_u32 s0, s24, s0
	v_lshlrev_b32_e32 v88, 4, v194
	v_mov_b32_e32 v89, v73
	s_addc_u32 s1, s25, s1
	v_lshl_add_u64 v[88:89], s[0:1], 0, v[88:89]
	s_mov_b64 s[0:1], 0x1c00
	s_ashr_i32 s29, s28, 31
	v_lshl_add_u64 v[88:89], v[88:89], 0, s[0:1]
	s_lshl_b64 s[6:7], s[28:29], 13
	s_lshl_b64 s[0:1], s[30:31], 12
	s_add_u32 s0, s26, s0
	v_lshlrev_b32_e32 v90, 3, v194
	v_mov_b32_e32 v91, v73
	s_addc_u32 s1, s27, s1
	v_lshl_add_u64 v[90:91], s[0:1], 0, v[90:91]
	s_mov_b64 s[0:1], 0x45c08000
	v_mov_b32_e32 v77, v73
	v_mov_b32_e32 v79, v73
	v_mov_b32_e32 v81, v73
	v_mov_b32_e32 v83, v73
	v_mov_b32_e32 v85, v73
	v_mov_b32_e32 v87, v73
	v_lshl_add_u64 v[90:91], v[90:91], 0, s[0:1]
	s_lshl_b64 s[10:11], s[28:29], 12
	s_mov_b32 s12, 0x3f9837f0
	v_mov_b32_e32 v93, 0x3727c5ac
	s_mov_b32 s13, 0xf800000
	v_mov_b32_e32 v95, 0x260
	s_movk_i32 s14, 0xf000
	v_mov_b32_e32 v118, 0xba000000
	v_mov_b32_e32 v119, 0x3a000000
	s_waitcnt vmcnt(0)
.LBB0_1219:
	v_ashrrev_i32_e32 v97, 31, v64
	v_mov_b32_e32 v96, v64
	v_ashrrev_i32_e32 v99, 31, v65
	v_mov_b32_e32 v98, v65
	v_ashrrev_i32_e32 v101, 31, v66
	v_mov_b32_e32 v100, v66
	v_ashrrev_i32_e32 v103, 31, v67
	v_mov_b32_e32 v102, v67
	v_lshlrev_b64 v[96:97], 11, v[96:97]
	v_lshlrev_b64 v[98:99], 11, v[98:99]
	v_lshlrev_b64 v[100:101], 11, v[100:101]
	v_lshlrev_b64 v[102:103], 11, v[102:103]
	v_lshl_add_u64 v[124:125], v[74:75], 0, v[96:97]
	v_lshl_add_u64 v[96:97], s[8:9], 0, v[96:97]
	v_mul_f32_e32 v94, 0x3d800000, v68
	v_mul_f32_e32 v92, 0x3d800000, v69
	v_mul_f32_e32 v64, 0x3d800000, v70
	v_mul_f32_e32 v68, 0x3d800000, v71
	global_load_dwordx2 v[66:67], v[90:91], off
	global_load_dwordx2 v[70:71], v[90:91], off offset:512
	global_load_dwordx2 v[104:105], v[90:91], off offset:1024
	global_load_dwordx2 v[108:109], v[90:91], off offset:1536
	global_load_dwordx2 v[110:111], v[90:91], off offset:2048
	global_load_dwordx2 v[112:113], v[90:91], off offset:2560
	global_load_dwordx2 v[114:115], v[90:91], off offset:3072
	global_load_dwordx2 v[116:117], v[90:91], off offset:3584
	v_lshl_add_u64 v[126:127], v[74:75], 0, v[98:99]
	v_lshl_add_u64 v[128:129], v[74:75], 0, v[100:101]
	v_lshl_add_u64 v[130:131], v[74:75], 0, v[102:103]
	global_load_dword v65, v[124:125], off
	global_load_dword v69, v[126:127], off
	global_load_dword v172, v[128:129], off
	global_load_dword v173, v[130:131], off
	v_lshl_add_u64 v[124:125], v[96:97], 0, v[72:73]
	s_add_i32 s0, s30, s28
	global_load_dword v174, v[124:125], off
	s_cmpk_lt_i32 s0, 0x4000
	s_cselect_b64 s[2:3], -1, 0
	s_and_b64 s[16:17], s[2:3], exec
	s_cselect_b32 s1, s0, s30
	v_lshl_add_u64 v[98:99], s[8:9], 0, v[98:99]
	s_mov_b32 s30, s0
	s_lshl_b32 s0, s1, 2
	v_lshl_add_u64 v[100:101], s[8:9], 0, v[100:101]
	v_lshl_add_u64 v[102:103], s[8:9], 0, v[102:103]
	v_lshl_add_u64 v[126:127], v[98:99], 0, v[72:73]
	s_ashr_i32 s1, s0, 31
	v_lshl_add_u64 v[128:129], v[100:101], 0, v[72:73]
	v_lshl_add_u64 v[130:131], v[102:103], 0, v[72:73]
	v_lshl_add_u64 v[132:133], v[96:97], 0, v[76:77]
	v_lshl_add_u64 v[134:135], v[98:99], 0, v[76:77]
	v_lshl_add_u64 v[136:137], v[100:101], 0, v[76:77]
	v_lshl_add_u64 v[138:139], v[102:103], 0, v[76:77]
	v_lshl_add_u64 v[140:141], v[96:97], 0, v[78:79]
	v_lshl_add_u64 v[142:143], v[98:99], 0, v[78:79]
	v_lshl_add_u64 v[144:145], v[100:101], 0, v[78:79]
	v_lshl_add_u64 v[146:147], v[102:103], 0, v[78:79]
	v_lshl_add_u64 v[148:149], v[96:97], 0, v[80:81]
	v_lshl_add_u64 v[150:151], v[98:99], 0, v[80:81]
	v_lshl_add_u64 v[152:153], v[100:101], 0, v[80:81]
	v_lshl_add_u64 v[154:155], v[102:103], 0, v[80:81]
	v_lshl_add_u64 v[156:157], v[96:97], 0, v[82:83]
	v_lshl_add_u64 v[158:159], v[98:99], 0, v[82:83]
	v_lshl_add_u64 v[160:161], v[100:101], 0, v[82:83]
	v_lshl_add_u64 v[162:163], v[102:103], 0, v[82:83]
	v_lshl_add_u64 v[164:165], v[96:97], 0, v[84:85]
	v_lshl_add_u64 v[166:167], v[98:99], 0, v[84:85]
; #define GAS __attribute__((address_space(1)))
; __global__ void __launch_bounds__(NTHR, 2) mk_fwd(Args args) {
;     ...
;             { const int mn = m + NGW < M ? m + NGW : m;
; #pragma unroll
;               for (int k = 0; k < 4; ++k) { nsl[k] = SLOT_OF[mn * 4 + k]; ngt[k] = GATE[mn * 4 + k]; } }
;             f32x4 v[8]; float s = 0.f;
; #pragma unroll
;             for (int q = 0; q < 8; ++q) { const int c = 4 * lane + 256 * q; f32x4 f = (f32x4){0.f, 0.f, 0.f, 0.f};
; #pragma unroll
;                 for (int k = 0; k < 4; ++k) { const unsigned yv = *(const GAS unsigned*)(YS + (size_t)sl[k] * D + c); const f32x2n lo2 = __builtin_amdgcn_cvt_pk_f32_fp8(yv, false), hi2 = __builtin_amdgcn_cvt_pk_f32_fp8(yv, true); f += (gt[k] * (1.0f / pg8::YS_SCALE)) * (f32x4){lo2.x, lo2.y, hi2.x, hi2.y}; }
	v_lshl_add_u64 v[168:169], v[100:101], 0, v[84:85]
	v_lshl_add_u64 v[170:171], v[102:103], 0, v[84:85]
	v_lshl_add_u64 v[96:97], v[96:97], 0, v[86:87]
	v_lshl_add_u64 v[98:99], v[98:99], 0, v[86:87]
	v_lshl_add_u64 v[100:101], v[100:101], 0, v[86:87]
	v_lshl_add_u64 v[102:103], v[102:103], 0, v[86:87]
	global_load_dword v175, v[126:127], off
	global_load_dword v176, v[128:129], off
	global_load_dword v177, v[130:131], off
	global_load_dword v178, v[132:133], off
	global_load_dword v179, v[134:135], off
	global_load_dword v182, v[136:137], off
	global_load_dword v186, v[138:139], off
	global_load_dword v190, v[140:141], off
	global_load_dword v194, v[142:143], off
	global_load_dword v198, v[144:145], off
	global_load_dword v202, v[146:147], off
	global_load_dword v206, v[148:149], off
	global_load_dword v210, v[150:151], off
	global_load_dword v214, v[152:153], off
	global_load_dword v218, v[154:155], off
	global_load_dword v222, v[156:157], off
	global_load_dword v226, v[158:159], off
	global_load_dword v230, v[160:161], off
	global_load_dword v234, v[162:163], off
	global_load_dword v238, v[164:165], off
	global_load_dword v242, v[166:167], off
	global_load_dword v246, v[168:169], off
	global_load_dword v248, v[170:171], off
	global_load_dword v244, v[96:97], off
	global_load_dword v249, v[98:99], off
	global_load_dword v250, v[100:101], off
	global_load_dword v251, v[102:103], off
	s_lshl_b64 s[0:1], s[0:1], 2
	s_add_u32 s16, s4, s0
	s_addc_u32 s17, s5, s1
	global_load_dwordx4 v[96:99], v73, s[16:17]
	s_add_u32 s18, s66, s0
	s_addc_u32 s19, s67, s1
	global_load_dwordx4 v[100:103], v73, s[18:19]
	v_mov_b32_e32 v120, 0
	v_mov_b32_e32 v121, 0
	s_and_b64 s[0:1], s[2:3], exec
	v_mov_b32_e32 v122, 0
	v_mov_b32_e32 v123, 0
	v_add_co_u32_e32 v106, vcc, s14, v88
	v_lshl_add_u64 v[90:91], v[90:91], 0, s[10:11]
	s_nop 0
	v_addc_co_u32_e32 v107, vcc, -1, v89, vcc
	s_waitcnt vmcnt(41)
	v_lshlrev_b32_e32 v124, 16, v66
	v_and_b32_e32 v125, 0xffff0000, v66
	v_lshlrev_b32_e32 v126, 16, v67
	v_and_b32_e32 v127, 0xffff0000, v67
	s_waitcnt vmcnt(40)
	v_lshlrev_b32_e32 v128, 16, v70
	v_and_b32_e32 v129, 0xffff0000, v70
	v_lshlrev_b32_e32 v70, 16, v71
	v_and_b32_e32 v71, 0xffff0000, v71
	s_waitcnt vmcnt(33)
	v_cvt_pk_f32_fp8_e32 v[66:67], v65
	v_cvt_pk_f32_fp8_sdwa v[142:143], v65 src0_sel:WORD_1
	s_waitcnt vmcnt(32)
	v_cvt_pk_f32_fp8_e32 v[144:145], v69
	v_cvt_pk_f32_fp8_sdwa v[146:147], v69 src0_sel:WORD_1
	s_waitcnt vmcnt(31)
	v_cvt_pk_f32_fp8_e32 v[148:149], v172
	v_cvt_pk_f32_fp8_sdwa v[150:151], v172 src0_sel:WORD_1
	s_waitcnt vmcnt(29)
	v_cvt_pk_f32_fp8_e32 v[156:157], v174
	v_cvt_pk_f32_fp8_e32 v[152:153], v173
	v_cvt_pk_f32_fp8_sdwa v[154:155], v173 src0_sel:WORD_1
	v_cvt_pk_f32_fp8_sdwa v[158:159], v174 src0_sel:WORD_1
	v_pk_fma_f32 v[66:67], v[66:67], v[94:95], 0 op_sel_hi:[1,0,0]
	v_pk_fma_f32 v[142:143], v[142:143], v[94:95], 0 op_sel_hi:[1,0,0]
	v_pk_fma_f32 v[66:67], v[144:145], v[92:93], v[66:67] op_sel_hi:[1,0,1]
	v_pk_fma_f32 v[142:143], v[146:147], v[92:93], v[142:143] op_sel_hi:[1,0,1]
	v_pk_fma_f32 v[156:157], v[156:157], v[94:95], 0 op_sel_hi:[1,0,0]
	v_pk_fma_f32 v[158:159], v[158:159], v[94:95], 0 op_sel_hi:[1,0,0]
	v_pk_fma_f32 v[142:143], v[150:151], v[64:65], v[142:143] op_sel_hi:[1,0,1]
	v_pk_fma_f32 v[66:67], v[148:149], v[64:65], v[66:67] op_sel_hi:[1,0,1]
	s_waitcnt vmcnt(28)
	v_cvt_pk_f32_fp8_e32 v[160:161], v175
	v_cvt_pk_f32_fp8_sdwa v[162:163], v175 src0_sel:WORD_1
	s_waitcnt vmcnt(27)
	v_cvt_pk_f32_fp8_e32 v[164:165], v176
	s_waitcnt vmcnt(25)
	v_cvt_pk_f32_fp8_e32 v[172:173], v178
	v_cvt_pk_f32_fp8_sdwa v[166:167], v176 src0_sel:WORD_1
	v_cvt_pk_f32_fp8_e32 v[168:169], v177
	v_cvt_pk_f32_fp8_sdwa v[170:171], v177 src0_sel:WORD_1
	s_waitcnt vmcnt(24)
	v_cvt_pk_f32_fp8_e32 v[176:177], v179
	v_cvt_pk_f32_fp8_sdwa v[174:175], v178 src0_sel:WORD_1
	v_cvt_pk_f32_fp8_sdwa v[178:179], v179 src0_sel:WORD_1
	s_waitcnt vmcnt(21)
	v_cvt_pk_f32_fp8_e32 v[188:189], v190
	v_cvt_pk_f32_fp8_sdwa v[190:191], v190 src0_sel:WORD_1
	s_waitcnt vmcnt(17)
	v_cvt_pk_f32_fp8_e32 v[204:205], v206
	v_cvt_pk_f32_fp8_sdwa v[206:207], v206 src0_sel:WORD_1
	v_cvt_pk_f32_fp8_e32 v[192:193], v194
	s_waitcnt vmcnt(13)
	v_cvt_pk_f32_fp8_e32 v[220:221], v222
	v_cvt_pk_f32_fp8_sdwa v[222:223], v222 src0_sel:WORD_1
	v_cvt_pk_f32_fp8_sdwa v[194:195], v194 src0_sel:WORD_1
	v_cvt_pk_f32_fp8_e32 v[208:209], v210
	s_waitcnt vmcnt(9)
	v_cvt_pk_f32_fp8_e32 v[236:237], v238
	v_cvt_pk_f32_fp8_sdwa v[238:239], v238 src0_sel:WORD_1
	v_cvt_pk_f32_fp8_sdwa v[210:211], v210 src0_sel:WORD_1
	v_cvt_pk_f32_fp8_e32 v[224:225], v226
	s_waitcnt vmcnt(5)
	v_cvt_pk_f32_fp8_e32 v[144:145], v244
	v_cvt_pk_f32_fp8_sdwa v[146:147], v244 src0_sel:WORD_1
	v_cvt_pk_f32_fp8_sdwa v[226:227], v226 src0_sel:WORD_1
	v_cvt_pk_f32_fp8_e32 v[240:241], v242
	v_cvt_pk_f32_fp8_sdwa v[242:243], v242 src0_sel:WORD_1
	v_pk_fma_f32 v[172:173], v[172:173], v[94:95], 0 op_sel_hi:[1,0,0]
	v_cvt_pk_f32_fp8_e32 v[150:151], v248
	v_cvt_pk_f32_fp8_sdwa v[148:149], v248 src0_sel:WORD_1
	v_pk_fma_f32 v[156:157], v[160:161], v[92:93], v[156:157] op_sel_hi:[1,0,1]
	s_waitcnt vmcnt(4)
	v_cvt_pk_f32_fp8_e32 v[160:161], v249
	v_cvt_pk_f32_fp8_sdwa v[248:249], v249 src0_sel:WORD_1
	v_cvt_pk_f32_fp8_e32 v[180:181], v182
	v_cvt_pk_f32_fp8_sdwa v[182:183], v182 src0_sel:WORD_1
	v_cvt_pk_f32_fp8_e32 v[196:197], v198
	v_cvt_pk_f32_fp8_sdwa v[198:199], v198 src0_sel:WORD_1
	v_cvt_pk_f32_fp8_e32 v[212:213], v214
	v_cvt_pk_f32_fp8_sdwa v[214:215], v214 src0_sel:WORD_1
	v_cvt_pk_f32_fp8_e32 v[228:229], v230
	v_cvt_pk_f32_fp8_sdwa v[230:231], v230 src0_sel:WORD_1
	v_cvt_pk_f32_fp8_e32 v[244:245], v246
	v_cvt_pk_f32_fp8_sdwa v[246:247], v246 src0_sel:WORD_1
	v_pk_fma_f32 v[158:159], v[162:163], v[92:93], v[158:159] op_sel_hi:[1,0,1]
	s_waitcnt vmcnt(3)
; #define GAS __attribute__((address_space(1)))
; __global__ void __launch_bounds__(NTHR, 2) mk_fwd(Args args) {
;     ...
;             for (int q = 0; q < 8; ++q) { const int c = 4 * lane + 256 * q; f32x4 f = (f32x4){0.f, 0.f, 0.f, 0.f};
; #pragma unroll
;                 for (int k = 0; k < 4; ++k) { const unsigned yv = *(const GAS unsigned*)(YS + (size_t)sl[k] * D + c); const f32x2n lo2 = __builtin_amdgcn_cvt_pk_f32_fp8(yv, false), hi2 = __builtin_amdgcn_cvt_pk_f32_fp8(yv, true); f += (gt[k] * (1.0f / pg8::YS_SCALE)) * (f32x4){lo2.x, lo2.y, hi2.x, hi2.y}; }
;                 { const v2u hw = *(const GAS v2u*)(H + (size_t)m * D + c); v[q] = ALPHA * (f32x4){bflo(hw.x), bfhi(hw.x), bflo(hw.y), bfhi(hw.y)} + f; } s += (v[q].x + v[q].y) + (v[q].z + v[q].w); }
	v_cvt_pk_f32_fp8_e32 v[162:163], v250
	v_pk_fma_f32 v[172:173], v[176:177], v[92:93], v[172:173] op_sel_hi:[1,0,1]
	v_cvt_pk_f32_fp8_sdwa v[176:177], v250 src0_sel:WORD_1
	v_cvt_pk_f32_fp8_e32 v[184:185], v186
	v_cvt_pk_f32_fp8_sdwa v[186:187], v186 src0_sel:WORD_1
	v_pk_fma_f32 v[174:175], v[174:175], v[94:95], 0 op_sel_hi:[1,0,0]
	v_cvt_pk_f32_fp8_e32 v[200:201], v202
	v_cvt_pk_f32_fp8_sdwa v[202:203], v202 src0_sel:WORD_1
	v_cvt_pk_f32_fp8_e32 v[216:217], v218
	v_cvt_pk_f32_fp8_sdwa v[218:219], v218 src0_sel:WORD_1
	v_cvt_pk_f32_fp8_e32 v[232:233], v234
	v_cvt_pk_f32_fp8_sdwa v[234:235], v234 src0_sel:WORD_1
	v_pk_fma_f32 v[190:191], v[190:191], v[94:95], 0 op_sel_hi:[1,0,0]
	v_pk_fma_f32 v[188:189], v[188:189], v[94:95], 0 op_sel_hi:[1,0,0]
	v_pk_fma_f32 v[206:207], v[206:207], v[94:95], 0 op_sel_hi:[1,0,0]
	v_pk_fma_f32 v[204:205], v[204:205], v[94:95], 0 op_sel_hi:[1,0,0]
	v_pk_fma_f32 v[222:223], v[222:223], v[94:95], 0 op_sel_hi:[1,0,0]
	v_pk_fma_f32 v[220:221], v[220:221], v[94:95], 0 op_sel_hi:[1,0,0]
	v_pk_fma_f32 v[238:239], v[238:239], v[94:95], 0 op_sel_hi:[1,0,0]
	v_pk_fma_f32 v[236:237], v[236:237], v[94:95], 0 op_sel_hi:[1,0,0]
	v_pk_fma_f32 v[146:147], v[146:147], v[94:95], 0 op_sel_hi:[1,0,0]
	v_pk_fma_f32 v[144:145], v[144:145], v[94:95], 0 op_sel_hi:[1,0,0]
	v_pk_fma_f32 v[174:175], v[178:179], v[92:93], v[174:175] op_sel_hi:[1,0,1]
	s_waitcnt vmcnt(2)
	v_cvt_pk_f32_fp8_e32 v[178:179], v251
	v_cvt_pk_f32_fp8_sdwa v[250:251], v251 src0_sel:WORD_1
	v_pk_fma_f32 v[188:189], v[192:193], v[92:93], v[188:189] op_sel_hi:[1,0,1]
	v_pk_fma_f32 v[190:191], v[194:195], v[92:93], v[190:191] op_sel_hi:[1,0,1]
	v_pk_fma_f32 v[192:193], v[208:209], v[92:93], v[204:205] op_sel_hi:[1,0,1]
	v_pk_fma_f32 v[194:195], v[210:211], v[92:93], v[206:207] op_sel_hi:[1,0,1]
	v_pk_fma_f32 v[204:205], v[224:225], v[92:93], v[220:221] op_sel_hi:[1,0,1]
	v_pk_fma_f32 v[206:207], v[226:227], v[92:93], v[222:223] op_sel_hi:[1,0,1]
	v_pk_fma_f32 v[208:209], v[240:241], v[92:93], v[236:237] op_sel_hi:[1,0,1]
	v_pk_fma_f32 v[210:211], v[242:243], v[92:93], v[238:239] op_sel_hi:[1,0,1]
	v_pk_fma_f32 v[144:145], v[160:161], v[92:93], v[144:145] op_sel_hi:[1,0,1]
	v_pk_fma_f32 v[146:147], v[248:249], v[92:93], v[146:147] op_sel_hi:[1,0,1]
	v_pk_fma_f32 v[152:153], v[152:153], v[68:69], v[66:67] op_sel_hi:[1,0,1]
	v_pk_fma_f32 v[142:143], v[154:155], v[68:69], v[142:143] op_sel_hi:[1,0,1]
	v_pk_fma_f32 v[154:155], v[166:167], v[64:65], v[158:159] op_sel_hi:[1,0,1]
	v_pk_fma_f32 v[156:157], v[164:165], v[64:65], v[156:157] op_sel_hi:[1,0,1]
	v_pk_fma_f32 v[158:159], v[182:183], v[64:65], v[174:175] op_sel_hi:[1,0,1]
	v_pk_fma_f32 v[160:161], v[180:181], v[64:65], v[172:173] op_sel_hi:[1,0,1]
	v_pk_fma_f32 v[164:165], v[198:199], v[64:65], v[190:191] op_sel_hi:[1,0,1]
	v_pk_fma_f32 v[166:167], v[196:197], v[64:65], v[188:189] op_sel_hi:[1,0,1]
	v_pk_fma_f32 v[172:173], v[214:215], v[64:65], v[194:195] op_sel_hi:[1,0,1]
	v_pk_fma_f32 v[174:175], v[212:213], v[64:65], v[192:193] op_sel_hi:[1,0,1]
	v_pk_fma_f32 v[180:181], v[230:231], v[64:65], v[206:207] op_sel_hi:[1,0,1]
	v_pk_fma_f32 v[182:183], v[228:229], v[64:65], v[204:205] op_sel_hi:[1,0,1]
	v_pk_fma_f32 v[188:189], v[246:247], v[64:65], v[210:211] op_sel_hi:[1,0,1]
	v_pk_fma_f32 v[190:191], v[244:245], v[64:65], v[208:209] op_sel_hi:[1,0,1]
	v_pk_fma_f32 v[146:147], v[176:177], v[64:65], v[146:147] op_sel_hi:[1,0,1]
	v_pk_fma_f32 v[144:145], v[162:163], v[64:65], v[144:145] op_sel_hi:[1,0,1]
	s_waitcnt vmcnt(1)
	v_mov_b64_e32 v[66:67], v[98:99]
	v_mov_b64_e32 v[64:65], v[96:97]
	v_pk_fma_f32 v[96:97], v[126:127], s[12:13], v[142:143] op_sel_hi:[1,0,1]
	v_pk_fma_f32 v[98:99], v[124:125], s[12:13], v[152:153] op_sel_hi:[1,0,1]
	v_pk_fma_f32 v[124:125], v[168:169], v[68:69], v[156:157] op_sel_hi:[1,0,1]
	v_pk_fma_f32 v[126:127], v[170:171], v[68:69], v[154:155] op_sel_hi:[1,0,1]
	v_lshlrev_b32_e32 v130, 16, v104
	v_and_b32_e32 v131, 0xffff0000, v104
	v_lshlrev_b32_e32 v104, 16, v105
	v_and_b32_e32 v105, 0xffff0000, v105
	v_pk_fma_f32 v[142:143], v[184:185], v[68:69], v[160:161] op_sel_hi:[1,0,1]
	v_pk_fma_f32 v[152:153], v[186:187], v[68:69], v[158:159] op_sel_hi:[1,0,1]
	v_pk_fma_f32 v[126:127], v[70:71], s[12:13], v[126:127] op_sel_hi:[1,0,1]
	v_pk_fma_f32 v[124:125], v[128:129], s[12:13], v[124:125] op_sel_hi:[1,0,1]
	v_lshlrev_b32_e32 v140, 16, v116
	v_and_b32_e32 v141, 0xffff0000, v116
	v_lshlrev_b32_e32 v116, 16, v117
	v_and_b32_e32 v117, 0xffff0000, v117
	v_pk_fma_f32 v[154:155], v[200:201], v[68:69], v[166:167] op_sel_hi:[1,0,1]
	v_pk_fma_f32 v[156:157], v[202:203], v[68:69], v[164:165] op_sel_hi:[1,0,1]
	v_pk_fma_f32 v[158:159], v[216:217], v[68:69], v[174:175] op_sel_hi:[1,0,1]
	v_pk_fma_f32 v[160:161], v[218:219], v[68:69], v[172:173] op_sel_hi:[1,0,1]
	v_pk_fma_f32 v[162:163], v[232:233], v[68:69], v[182:183] op_sel_hi:[1,0,1]
	v_pk_fma_f32 v[164:165], v[234:235], v[68:69], v[180:181] op_sel_hi:[1,0,1]
	v_pk_fma_f32 v[150:151], v[150:151], v[68:69], v[190:191] op_sel_hi:[1,0,1]
	v_pk_fma_f32 v[148:149], v[148:149], v[68:69], v[188:189] op_sel_hi:[1,0,1]
	v_pk_fma_f32 v[144:145], v[178:179], v[68:69], v[144:145] op_sel_hi:[1,0,1]
	v_pk_fma_f32 v[68:69], v[250:251], v[68:69], v[146:147] op_sel_hi:[1,0,1]
	v_mov_b32_e32 v128, v98
	v_mov_b32_e32 v146, v99
	v_mov_b32_e32 v166, v96
	v_mov_b32_e32 v168, v97
	v_pk_fma_f32 v[104:105], v[104:105], s[12:13], v[152:153] op_sel_hi:[1,0,1]
	v_pk_fma_f32 v[130:131], v[130:131], s[12:13], v[142:143] op_sel_hi:[1,0,1]
	v_mov_b32_e32 v129, v124
	v_mov_b32_e32 v147, v125
	v_mov_b32_e32 v167, v126
	v_mov_b32_e32 v169, v127
	v_pk_fma_f32 v[116:117], v[116:117], s[12:13], v[68:69] op_sel_hi:[1,0,1]
	s_waitcnt vmcnt(0)
; #define GAS __attribute__((address_space(1)))
; __device__ __forceinline__ float wave_sum_dpp(float x) {
;     x = row16_sum(x);
;     x += __builtin_bit_cast(float, __builtin_amdgcn_update_dpp(0, __builtin_bit_cast(int, x), 0x142, 0xA, 0xF, false));
;     x += __builtin_bit_cast(float, __builtin_amdgcn_update_dpp(0, __builtin_bit_cast(int, x), 0x143, 0xC, 0xF, false));
;     return __builtin_bit_cast(float, __builtin_amdgcn_readlane(__builtin_bit_cast(int, x), 63));
; __global__ void __launch_bounds__(NTHR, 2) mk_fwd(Args args) {
;     ...
;                 { const v2u hw = *(const GAS v2u*)(H + (size_t)m * D + c); v[q] = ALPHA * (f32x4){bflo(hw.x), bfhi(hw.x), bflo(hw.y), bfhi(hw.y)} + f; } s += (v[q].x + v[q].y) + (v[q].z + v[q].w); }
;             const float mean = wave_sum_dpp(s) * (1.0f / D); float s2 = 0.f;
; #pragma unroll
;             for (int q = 0; q < 8; ++q) { v[q] = v[q] - mean; s2 += (v[q].x * v[q].x + v[q].y * v[q].y) + (v[q].z * v[q].z + v[q].w * v[q].w); }
	v_mov_b64_e32 v[70:71], v[102:103]
	v_mov_b64_e32 v[68:69], v[100:101]
	v_pk_mov_b32 v[100:101], v[130:131], v[104:105] op_sel:[1,0]
	v_mov_b32_e32 v102, v130
	v_mov_b32_e32 v103, v105
	v_pk_add_f32 v[128:129], v[128:129], v[146:147]
	v_pk_add_f32 v[146:147], v[166:167], v[168:169]
	v_lshlrev_b32_e32 v132, 16, v108
	v_and_b32_e32 v133, 0xffff0000, v108
	v_lshlrev_b32_e32 v108, 16, v109
	v_and_b32_e32 v109, 0xffff0000, v109
	v_lshlrev_b32_e32 v134, 16, v110
	v_and_b32_e32 v135, 0xffff0000, v110
	v_lshlrev_b32_e32 v110, 16, v111
	v_and_b32_e32 v111, 0xffff0000, v111
	v_pk_add_f32 v[100:101], v[100:101], v[102:103]
	v_pk_add_f32 v[128:129], v[128:129], v[146:147]
	v_lshlrev_b32_e32 v136, 16, v112
	v_and_b32_e32 v137, 0xffff0000, v112
	v_lshlrev_b32_e32 v112, 16, v113
	v_and_b32_e32 v113, 0xffff0000, v113
	v_lshlrev_b32_e32 v138, 16, v114
	v_and_b32_e32 v139, 0xffff0000, v114
	v_lshlrev_b32_e32 v114, 16, v115
	v_and_b32_e32 v115, 0xffff0000, v115
	v_pk_fma_f32 v[108:109], v[108:109], s[12:13], v[156:157] op_sel_hi:[1,0,1]
	v_pk_fma_f32 v[132:133], v[132:133], s[12:13], v[154:155] op_sel_hi:[1,0,1]
	v_pk_fma_f32 v[110:111], v[110:111], s[12:13], v[160:161] op_sel_hi:[1,0,1]
	v_pk_fma_f32 v[134:135], v[134:135], s[12:13], v[158:159] op_sel_hi:[1,0,1]
	v_pk_add_f32 v[100:101], v[100:101], v[100:101] op_sel:[0,1] op_sel_hi:[1,0]
	v_add_f32_e32 v92, 0, v128
	v_pk_fma_f32 v[112:113], v[112:113], s[12:13], v[164:165] op_sel_hi:[1,0,1]
	v_pk_fma_f32 v[136:137], v[136:137], s[12:13], v[162:163] op_sel_hi:[1,0,1]
	v_pk_fma_f32 v[114:115], v[114:115], s[12:13], v[148:149] op_sel_hi:[1,0,1]
	v_pk_fma_f32 v[140:141], v[140:141], s[12:13], v[144:145] op_sel_hi:[1,0,1]
	v_add_f32_e32 v142, v132, v133
	v_add_f32_e32 v144, v108, v109
	v_mov_b32_e32 v149, v134
	v_mov_b32_e32 v143, v110
	v_mov_b32_e32 v145, v111
	v_mov_b32_e32 v101, v135
	v_add_f32_e32 v148, v92, v129
	v_pk_fma_f32 v[138:139], v[138:139], s[12:13], v[150:151] op_sel_hi:[1,0,1]
	v_pk_mov_b32 v[150:151], v[136:137], v[112:113] op_sel:[1,0]
	v_mov_b32_e32 v152, v136
	v_mov_b32_e32 v153, v113
	v_pk_add_f32 v[102:103], v[142:143], v[144:145]
	v_pk_add_f32 v[100:101], v[148:149], v[100:101]
	v_pk_add_f32 v[142:143], v[150:151], v[152:153]
	v_pk_add_f32 v[100:101], v[100:101], v[102:103]
	v_pk_add_f32 v[142:143], v[142:143], v[142:143] op_sel:[0,1] op_sel_hi:[1,0]
	v_pk_add_f32 v[100:101], v[100:101], v[100:101] op_sel:[0,1] op_sel_hi:[1,0]
	v_add_f32_e32 v154, v138, v139
	v_add_f32_e32 v156, v114, v115
	v_mov_b32_e32 v155, v116
	v_mov_b32_e32 v157, v117
	v_mov_b32_e32 v143, v141
	v_mov_b32_e32 v101, v140
	v_pk_add_f32 v[144:145], v[154:155], v[156:157]
	v_pk_add_f32 v[100:101], v[100:101], v[142:143]
	s_nop 0
	v_pk_add_f32 v[100:101], v[100:101], v[144:145]
	s_nop 0
	v_add_f32_e32 v92, v100, v101
	s_nop 1
	v_add_f32_dpp v92, v92, v92 quad_perm:[1,0,3,2] row_mask:0xf bank_mask:0xf bound_ctrl:1
	s_nop 1
	v_add_f32_dpp v92, v92, v92 quad_perm:[2,3,0,1] row_mask:0xf bank_mask:0xf bound_ctrl:1
	s_nop 1
	v_add_f32_dpp v92, v92, v92 row_half_mirror row_mask:0xf bank_mask:0xf bound_ctrl:1
	s_nop 1
	v_add_f32_dpp v92, v92, v92 row_mirror row_mask:0xf bank_mask:0xf bound_ctrl:1
	s_nop 1
	v_mov_b32_dpp v120, v92 row_bcast:15 row_mask:0xa bank_mask:0xf
	v_add_f32_e32 v92, v92, v120
	s_nop 1
	v_mov_b32_dpp v121, v92 row_bcast:31 row_mask:0xc bank_mask:0xf
	v_add_f32_e32 v92, v92, v121
	s_nop 0
	v_readlane_b32 s2, v92, 63
	s_nop 1
	v_fmac_f32_e32 v97, s2, v118
	v_fmac_f32_e32 v99, s2, v118
	v_fmac_f32_e32 v127, s2, v118
	v_fmac_f32_e32 v125, s2, v118
	v_fma_f32 v96, s2, v118, v96
	v_fma_f32 v98, s2, v118, v98
	v_fma_f32 v126, s2, v118, v126
	v_fma_f32 v124, s2, v118, v124
	v_fmac_f32_e32 v105, s2, v118
	v_fmac_f32_e32 v131, s2, v118
	v_mul_f32_e32 v92, v99, v99
	v_mul_f32_e32 v94, v97, v97
	v_mul_f32_e32 v100, v125, v125
	v_mul_f32_e32 v101, v127, v127
	v_fma_f32 v104, s2, v118, v104
	v_fma_f32 v130, s2, v118, v130
	v_fmac_f32_e32 v109, s2, v118
	v_fmac_f32_e32 v133, s2, v118
	v_mul_f32_e32 v102, v131, v131
	v_mul_f32_e32 v103, v105, v105
	v_fmac_f32_e32 v92, v98, v98
	v_fmac_f32_e32 v94, v96, v96
	v_fmac_f32_e32 v100, v124, v124
	v_fmac_f32_e32 v101, v126, v126
	v_fma_f32 v108, s2, v118, v108
	v_fma_f32 v132, s2, v118, v132
	v_fmac_f32_e32 v111, s2, v118
	v_fmac_f32_e32 v135, s2, v118
	v_mul_f32_e32 v120, v133, v133
	v_mul_f32_e32 v121, v109, v109
	v_fmac_f32_e32 v102, v130, v130
	v_fmac_f32_e32 v103, v104, v104
	v_add_f32_e32 v92, v92, v94
	v_add_f32_e32 v94, v100, v101
	v_fma_f32 v110, s2, v118, v110
	v_fma_f32 v134, s2, v118, v134
	v_fmac_f32_e32 v113, s2, v118
	v_fmac_f32_e32 v137, s2, v118
	v_mul_f32_e32 v128, v135, v135
	v_mul_f32_e32 v129, v111, v111
	v_fmac_f32_e32 v120, v132, v132
	v_fmac_f32_e32 v121, v108, v108
	v_add_f32_e32 v100, v102, v103
	v_add_f32_e32 v92, v92, v94
	v_fma_f32 v112, s2, v118, v112
	v_fma_f32 v136, s2, v118, v136
	v_fmac_f32_e32 v115, s2, v118
	v_fmac_f32_e32 v139, s2, v118
	v_mul_f32_e32 v142, v137, v137
	v_mul_f32_e32 v143, v113, v113
	v_fmac_f32_e32 v128, v134, v134
	v_fmac_f32_e32 v129, v110, v110
	v_add_f32_e32 v101, v120, v121
	v_add_f32_e32 v92, v92, v100
; #define GAS __attribute__((address_space(1)))
; #define LAS __attribute__((address_space(3)))
; __global__ void __launch_bounds__(NTHR, 2) mk_fwd(Args args) {
;     ...
;             const float mean = wave_sum_dpp(s) * (1.0f / D); float s2 = 0.f;
; #pragma unroll
;             for (int q = 0; q < 8; ++q) { v[q] = v[q] - mean; s2 += (v[q].x * v[q].x + v[q].y * v[q].y) + (v[q].z * v[q].z + v[q].w * v[q].w); }
;             const float rstd = 1.0f / sqrtf(wave_sum_dpp(s2) * (1.0f / D) + LN_EPS);
; #pragma unroll
;             for (int q = 0; q < 8; ++q) { const int c = 4 * lane + 256 * q; *(GAS f32x4*)(out + (size_t)m * D + c) = v[q] * rstd * *(const LAS f32x4*)(s_lnw + c) + *(const LAS f32x4*)(s_lnb + c); }
	v_fma_f32 v114, s2, v118, v114
	v_fma_f32 v138, s2, v118, v138
	v_fmac_f32_e32 v117, s2, v118
	v_fmac_f32_e32 v141, s2, v118
	v_mul_f32_e32 v144, v139, v139
	v_mul_f32_e32 v145, v115, v115
	v_fmac_f32_e32 v142, v136, v136
	v_fmac_f32_e32 v143, v112, v112
	v_add_f32_e32 v102, v128, v129
	v_add_f32_e32 v92, v92, v101
	v_fma_f32 v116, s2, v118, v116
	v_fma_f32 v140, s2, v118, v140
	v_mul_f32_e32 v146, v141, v141
	v_mul_f32_e32 v147, v117, v117
	v_fmac_f32_e32 v144, v138, v138
	v_fmac_f32_e32 v145, v114, v114
	v_add_f32_e32 v103, v142, v143
	v_add_f32_e32 v92, v92, v102
	v_fmac_f32_e32 v146, v140, v140
	v_fmac_f32_e32 v147, v116, v116
	v_add_f32_e32 v120, v144, v145
	v_add_f32_e32 v92, v92, v103
	v_add_f32_e32 v121, v146, v147
	v_add_f32_e32 v92, v92, v120
	v_add_f32_e32 v92, v92, v121
	s_nop 1
	v_add_f32_dpp v92, v92, v92 quad_perm:[1,0,3,2] row_mask:0xf bank_mask:0xf bound_ctrl:1
	s_nop 1
	v_add_f32_dpp v92, v92, v92 quad_perm:[2,3,0,1] row_mask:0xf bank_mask:0xf bound_ctrl:1
	s_nop 1
	v_add_f32_dpp v92, v92, v92 row_half_mirror row_mask:0xf bank_mask:0xf bound_ctrl:1
	s_nop 1
	v_add_f32_dpp v92, v92, v92 row_mirror row_mask:0xf bank_mask:0xf bound_ctrl:1
	s_nop 1
	v_mov_b32_dpp v122, v92 row_bcast:15 row_mask:0xa bank_mask:0xf
	v_add_f32_e32 v92, v92, v122
	s_nop 1
	v_mov_b32_dpp v123, v92 row_bcast:31 row_mask:0xc bank_mask:0xf
	v_add_f32_e32 v92, v92, v123
	s_nop 0
	v_readlane_b32 s2, v92, 63
	s_nop 1
	v_fma_f32 v92, s2, v119, v93
	v_mul_f32_e32 v94, 0x4f800000, v92
	v_cmp_gt_f32_e32 vcc, s13, v92
	s_nop 1
	v_cndmask_b32_e32 v92, v92, v94, vcc
	v_sqrt_f32_e32 v94, v92
	s_nop 0
	v_add_u32_e32 v100, -1, v94
	v_add_u32_e32 v101, 1, v94
	v_fma_f32 v102, -v100, v94, v92
	v_fma_f32 v103, -v101, v94, v92
	v_cmp_ge_f32_e64 s[2:3], 0, v102
	s_nop 1
	v_cndmask_b32_e64 v94, v94, v100, s[2:3]
	v_cmp_lt_f32_e64 s[2:3], 0, v103
	s_nop 1
	v_cndmask_b32_e64 v94, v94, v101, s[2:3]
	v_mul_f32_e32 v100, 0x37800000, v94
	v_cndmask_b32_e32 v94, v94, v100, vcc
	v_cmp_class_f32_e32 vcc, v92, v95
	s_nop 1
	v_cndmask_b32_e32 v92, v94, v92, vcc
	v_div_scale_f32 v94, s[2:3], v92, v92, 1.0
	v_rcp_f32_e32 v101, v94
	v_div_scale_f32 v100, vcc, 1.0, v92, 1.0
	v_fma_f32 v102, -v94, v101, 1.0
	v_fmac_f32_e32 v101, v102, v101
	v_mul_f32_e32 v102, v100, v101
	v_fma_f32 v103, -v94, v102, v100
	v_fmac_f32_e32 v102, v103, v101
	v_fma_f32 v94, -v94, v102, v100
	v_div_fmas_f32 v94, v94, v101, v102
	v_div_fixup_f32 v92, v94, v92, 1.0
	v_pk_mul_f32 v[100:101], v[92:93], v[98:99] op_sel_hi:[0,1]
	v_pk_mul_f32 v[96:97], v[92:93], v[96:97] op_sel_hi:[0,1]
	v_pk_mul_f32 v[120:121], v[92:93], v[124:125] op_sel_hi:[0,1]
	v_pk_mul_f32 v[102:103], v[92:93], v[126:127] op_sel_hi:[0,1]
	v_pk_mul_f32 v[122:123], v[92:93], v[130:131] op_sel_hi:[0,1]
	v_pk_mul_f32 v[104:105], v[92:93], v[104:105] op_sel_hi:[0,1]
	v_pk_mul_f32 v[124:125], v[92:93], v[132:133] op_sel_hi:[0,1]
	v_pk_mul_f32 v[126:127], v[92:93], v[108:109] op_sel_hi:[0,1]
	v_pk_mul_f32 v[128:129], v[92:93], v[134:135] op_sel_hi:[0,1]
	v_pk_mul_f32 v[130:131], v[92:93], v[110:111] op_sel_hi:[0,1]
	v_pk_mul_f32 v[132:133], v[92:93], v[136:137] op_sel_hi:[0,1]
	v_pk_mul_f32 v[134:135], v[92:93], v[112:113] op_sel_hi:[0,1]
	v_pk_mul_f32 v[136:137], v[92:93], v[138:139] op_sel_hi:[0,1]
	v_pk_mul_f32 v[138:139], v[92:93], v[114:115] op_sel_hi:[0,1]
	v_pk_mul_f32 v[140:141], v[92:93], v[140:141] op_sel_hi:[0,1]
	v_pk_mul_f32 v[116:117], v[92:93], v[116:117] op_sel_hi:[0,1]
	s_waitcnt lgkmcnt(13)
	v_pk_fma_f32 v[98:99], v[96:97], v[2:3], v[10:11]
	v_pk_fma_f32 v[96:97], v[100:101], v[0:1], v[8:9]
	s_waitcnt lgkmcnt(12)
	v_pk_fma_f32 v[102:103], v[102:103], v[6:7], v[14:15]
	v_pk_fma_f32 v[100:101], v[120:121], v[4:5], v[12:13]
	s_waitcnt lgkmcnt(9)
	v_pk_fma_f32 v[110:111], v[104:105], v[18:19], v[26:27]
	v_pk_fma_f32 v[108:109], v[122:123], v[16:17], v[24:25]
	s_waitcnt lgkmcnt(8)
	v_pk_fma_f32 v[114:115], v[126:127], v[22:23], v[30:31]
	v_pk_fma_f32 v[112:113], v[124:125], v[20:21], v[28:29]
	s_waitcnt lgkmcnt(5)
	v_pk_fma_f32 v[122:123], v[130:131], v[34:35], v[42:43]
	v_pk_fma_f32 v[120:121], v[128:129], v[32:33], v[40:41]
	s_waitcnt lgkmcnt(4)
	v_pk_fma_f32 v[126:127], v[134:135], v[38:39], v[46:47]
	v_pk_fma_f32 v[124:125], v[132:133], v[36:37], v[44:45]
	s_waitcnt lgkmcnt(1)
	v_pk_fma_f32 v[130:131], v[138:139], v[50:51], v[58:59]
	v_pk_fma_f32 v[128:129], v[136:137], v[48:49], v[56:57]
	s_waitcnt lgkmcnt(0)
	v_pk_fma_f32 v[134:135], v[116:117], v[54:55], v[62:63]
	v_pk_fma_f32 v[132:133], v[140:141], v[52:53], v[60:61]
	global_store_dwordx4 v[106:107], v[96:99], off offset:-3072 nt
	global_store_dwordx4 v[106:107], v[100:103], off offset:-2048 nt
	global_store_dwordx4 v[106:107], v[108:111], off offset:-1024 nt
	global_store_dwordx4 v[88:89], v[112:115], off offset:-4096 nt
	global_store_dwordx4 v[88:89], v[120:123], off offset:-3072 nt
	global_store_dwordx4 v[88:89], v[124:127], off offset:-2048 nt
	global_store_dwordx4 v[88:89], v[128:131], off offset:-1024 nt
	global_store_dwordx4 v[88:89], v[132:135], off nt
	v_lshl_add_u64 v[88:89], v[88:89], 0, s[6:7]
	s_mov_b64 vcc, s[0:1]
	s_cbranch_vccnz .LBB0_1219
